# GU phase row-table fill: all row-index loads in flight before the LDS stores (was one exposed load per unit)
# speedup vs baseline: 1.0084x; 1.0050x over previous
;   __device__ __forceinline__ bool next(int i,AttnUnit&u)const{ const int pair=vcu+(i>>1)*G; if(pair>=256)return false; const int s=pair&15; u.bh=pair>>4; u.qb=(i&1)?31-s:s; return true; }
;     __device__ __forceinline__ bool next(int i, Unit& u) const { return i == 0 && so.next(round, u); }
;     __device__ __forceinline__ bool next(int i, Unit& u) const {
;         int ul = i * (G >> 3) + (c >> 3);
;         if (ul >= xt[4]) return false;
;         const int s = (ul >= xt[1] ? 1 : 0) + (ul >= xt[2] ? 1 : 0) + (ul >= xt[3] ? 1 : 0);
;         ul -= xt[s];
;         u.pm = xt[8 + s] + (ul >> 2); u.pn = 4 * ((c & 7) + 8 * s) + (ul & 3); return true;
;     }
; __global__ void __launch_bounds__(NWAVES * 64, 2) mega_fwd(Args args) {
;     ...
;             { pg8::Unit u_; const int* rowtok = (const int*)(F.ws + WS_SMALL + 512 * 1024);
;               const int nxu_ = __builtin_amdgcn_readfirstlane(TS[44]), lcu_ = F.bx >> 3, peru_ = F.G >> 3; int nu_ = nxu_ > lcu_ ? (nxu_ - lcu_ + peru_ - 1) / peru_ : 0; nu_ = nu_ > 12 ? 12 : nu_;
;               _Pragma("unroll 1") for (int i_ = 0; i_ < nu_; ++i_) { (void)S.next(i_, u_); const int pm_ = __builtin_amdgcn_readfirstlane(u_.pm);
;                   if (F.tid < 256) { const unsigned tk = (unsigned)rowtok[pm_ * 256 + F.tid]; RT[i_ * 256 + F.tid] = (int)(tk < (unsigned)T ? tk : (unsigned)(T - 1)); } } }
.LBB0_3515:
	s_add_i32 s37, s30, 0x204a0
	s_add_i32 s38, s30, 0x21000
	s_cmp_lt_i32 s13, 1
	s_cbranch_scc1 .LBB0_3522
	s_add_u32 s4, s8, 0x380000
	s_movk_i32 s0, 0x100
	v_lshl_add_u32 v1, v132, 2, s38
	s_addc_u32 s5, s9, 0
	s_ashr_i32 s14, s28, 3
	s_add_i32 s15, s30, 0x204a4
	s_add_i32 s16, s30, 0x204ac
	v_cmp_gt_i32_e64 s[0:1], s0, v132
	s_mov_b32 s17, s36
	s_branch .LBB0_3518
.LBB0_3518:
	v_mov_b32_e32 v0, s35
	ds_read_b32 v0, v0
	s_waitcnt lgkmcnt(0)
	v_cmp_ge_i32_e32 vcc, s17, v0
	s_cbranch_vccnz .Lmy_rt_d0
	v_mov_b32_e32 v0, s15
	ds_read2_b32 v[4:5], v0 offset1:1
	v_mov_b32_e32 v0, s16
	ds_read_b32 v0, v0
	s_waitcnt lgkmcnt(1)
	v_cmp_ge_i32_e32 vcc, s17, v4
	s_nop 1
	v_cndmask_b32_e64 v2, 0, 1, vcc
	v_cmp_ge_i32_e32 vcc, s17, v5
	v_lshlrev_b32_e32 v2, 2, v2
	s_nop 0
	v_cndmask_b32_e64 v4, 0, 1, vcc
	s_waitcnt lgkmcnt(0)
	v_cmp_ge_i32_e32 vcc, s17, v0
	v_lshlrev_b32_e32 v4, 2, v4
	v_add_u32_e32 v4, s37, v4
	v_cndmask_b32_e64 v0, 0, 1, vcc
	v_add_u32_e32 v2, v4, v2
	v_lshlrev_b32_e32 v0, 2, v0
	v_add_u32_e32 v0, v2, v0
	ds_read2_b32 v[4:5], v0 offset1:8
	s_waitcnt lgkmcnt(0)
	v_sub_u32_e32 v0, s17, v4
	v_ashrrev_i32_e32 v0, 2, v0
	v_add_u32_e32 v236, v0, v5
.Lmy_rt_d0:
	s_nop 0
	v_readfirstlane_b32 s18, v236
	s_and_saveexec_b64 s[10:11], s[0:1]
	v_lshl_add_u32 v4, s18, 8, v132
	v_ashrrev_i32_e32 v5, 31, v4
	v_lshl_add_u64 v[4:5], v[4:5], 2, s[4:5]
	global_load_dword v6, v[4:5], off
	s_or_b64 exec, exec, s[10:11]
	s_add_i32 s13, s13, -1
	s_add_i32 s17, s17, s14
	s_cmp_eq_u32 s13, 0
	s_cbranch_scc1 .Lmy_rt_g0

;   __device__ __forceinline__ bool next(int i,AttnUnit&u)const{ const int pair=vcu+(i>>1)*G; if(pair>=256)return false; const int s=pair&15; u.bh=pair>>4; u.qb=(i&1)?31-s:s; return true; }
;     __device__ __forceinline__ bool next(int i, Unit& u) const { return i == 0 && so.next(round, u); }
; __global__ void __launch_bounds__(NWAVES * 64, 2) mega_fwd(Args args) {
;     ...
;               _Pragma("unroll 1") for (int i_ = 0; i_ < nu_; ++i_) { (void)S.next(i_, u_); const int pm_ = __builtin_amdgcn_readfirstlane(u_.pm);
;                   if (F.tid < 256) { const unsigned tk = (unsigned)rowtok[pm_ * 256 + F.tid]; RT[i_ * 256 + F.tid] = (int)(tk < (unsigned)T ? tk : (unsigned)(T - 1)); } } }
.Lmy_rt_d1:
	s_nop 0
	v_readfirstlane_b32 s18, v236
	s_and_saveexec_b64 s[10:11], s[0:1]
	v_lshl_add_u32 v4, s18, 8, v132
	v_ashrrev_i32_e32 v5, 31, v4
	v_lshl_add_u64 v[4:5], v[4:5], 2, s[4:5]
	global_load_dword v7, v[4:5], off
	s_or_b64 exec, exec, s[10:11]
	s_add_i32 s13, s13, -1
	s_add_i32 s17, s17, s14
	s_cmp_eq_u32 s13, 0
	s_cbranch_scc1 .Lmy_rt_g1

;   __device__ __forceinline__ bool next(int i,AttnUnit&u)const{ const int pair=vcu+(i>>1)*G; if(pair>=256)return false; const int s=pair&15; u.bh=pair>>4; u.qb=(i&1)?31-s:s; return true; }
;     __device__ __forceinline__ bool next(int i, Unit& u) const { return i == 0 && so.next(round, u); }
; __global__ void __launch_bounds__(NWAVES * 64, 2) mega_fwd(Args args) {
;     ...
;               _Pragma("unroll 1") for (int i_ = 0; i_ < nu_; ++i_) { (void)S.next(i_, u_); const int pm_ = __builtin_amdgcn_readfirstlane(u_.pm);
;                   if (F.tid < 256) { const unsigned tk = (unsigned)rowtok[pm_ * 256 + F.tid]; RT[i_ * 256 + F.tid] = (int)(tk < (unsigned)T ? tk : (unsigned)(T - 1)); } } }
.Lmy_rt_d2:
	s_nop 0
	v_readfirstlane_b32 s18, v236
	s_and_saveexec_b64 s[10:11], s[0:1]
	v_lshl_add_u32 v4, s18, 8, v132
	v_ashrrev_i32_e32 v5, 31, v4
	v_lshl_add_u64 v[4:5], v[4:5], 2, s[4:5]
	global_load_dword v8, v[4:5], off
	s_or_b64 exec, exec, s[10:11]
	s_add_i32 s13, s13, -1
	s_add_i32 s17, s17, s14
	s_cmp_eq_u32 s13, 0
	s_cbranch_scc1 .Lmy_rt_g2

;   __device__ __forceinline__ bool next(int i,AttnUnit&u)const{ const int pair=vcu+(i>>1)*G; if(pair>=256)return false; const int s=pair&15; u.bh=pair>>4; u.qb=(i&1)?31-s:s; return true; }
;     __device__ __forceinline__ bool next(int i, Unit& u) const { return i == 0 && so.next(round, u); }
; __global__ void __launch_bounds__(NWAVES * 64, 2) mega_fwd(Args args) {
;     ...
;               _Pragma("unroll 1") for (int i_ = 0; i_ < nu_; ++i_) { (void)S.next(i_, u_); const int pm_ = __builtin_amdgcn_readfirstlane(u_.pm);
;                   if (F.tid < 256) { const unsigned tk = (unsigned)rowtok[pm_ * 256 + F.tid]; RT[i_ * 256 + F.tid] = (int)(tk < (unsigned)T ? tk : (unsigned)(T - 1)); } } }
.Lmy_rt_d3:
	s_nop 0
	v_readfirstlane_b32 s18, v236
	s_and_saveexec_b64 s[10:11], s[0:1]
	v_lshl_add_u32 v4, s18, 8, v132
	v_ashrrev_i32_e32 v5, 31, v4
	v_lshl_add_u64 v[4:5], v[4:5], 2, s[4:5]
	global_load_dword v9, v[4:5], off
	s_or_b64 exec, exec, s[10:11]
	s_add_i32 s13, s13, -1
	s_add_i32 s17, s17, s14
	s_cmp_eq_u32 s13, 0
	s_cbranch_scc1 .Lmy_rt_g3

;   __device__ __forceinline__ bool next(int i,AttnUnit&u)const{ const int pair=vcu+(i>>1)*G; if(pair>=256)return false; const int s=pair&15; u.bh=pair>>4; u.qb=(i&1)?31-s:s; return true; }
;     __device__ __forceinline__ bool next(int i, Unit& u) const { return i == 0 && so.next(round, u); }
; __global__ void __launch_bounds__(NWAVES * 64, 2) mega_fwd(Args args) {
;     ...
;               _Pragma("unroll 1") for (int i_ = 0; i_ < nu_; ++i_) { (void)S.next(i_, u_); const int pm_ = __builtin_amdgcn_readfirstlane(u_.pm);
;                   if (F.tid < 256) { const unsigned tk = (unsigned)rowtok[pm_ * 256 + F.tid]; RT[i_ * 256 + F.tid] = (int)(tk < (unsigned)T ? tk : (unsigned)(T - 1)); } } }
.Lmy_rt_d4:
	s_nop 0
	v_readfirstlane_b32 s18, v236
	s_and_saveexec_b64 s[10:11], s[0:1]
	v_lshl_add_u32 v4, s18, 8, v132
	v_ashrrev_i32_e32 v5, 31, v4
	v_lshl_add_u64 v[4:5], v[4:5], 2, s[4:5]
	global_load_dword v10, v[4:5], off
	s_or_b64 exec, exec, s[10:11]
	s_add_i32 s13, s13, -1
	s_add_i32 s17, s17, s14
	s_cmp_eq_u32 s13, 0
	s_cbranch_scc1 .Lmy_rt_g4

;   __device__ __forceinline__ bool next(int i,AttnUnit&u)const{ const int pair=vcu+(i>>1)*G; if(pair>=256)return false; const int s=pair&15; u.bh=pair>>4; u.qb=(i&1)?31-s:s; return true; }
;     __device__ __forceinline__ bool next(int i, Unit& u) const { return i == 0 && so.next(round, u); }
; __global__ void __launch_bounds__(NWAVES * 64, 2) mega_fwd(Args args) {
;     ...
;               _Pragma("unroll 1") for (int i_ = 0; i_ < nu_; ++i_) { (void)S.next(i_, u_); const int pm_ = __builtin_amdgcn_readfirstlane(u_.pm);
;                   if (F.tid < 256) { const unsigned tk = (unsigned)rowtok[pm_ * 256 + F.tid]; RT[i_ * 256 + F.tid] = (int)(tk < (unsigned)T ? tk : (unsigned)(T - 1)); } } }
.Lmy_rt_d5:
	s_nop 0
	v_readfirstlane_b32 s18, v236
	s_and_saveexec_b64 s[10:11], s[0:1]
	v_lshl_add_u32 v4, s18, 8, v132
	v_ashrrev_i32_e32 v5, 31, v4
	v_lshl_add_u64 v[4:5], v[4:5], 2, s[4:5]
	global_load_dword v11, v[4:5], off
	s_or_b64 exec, exec, s[10:11]
	s_add_i32 s13, s13, -1
	s_add_i32 s17, s17, s14
	s_cmp_eq_u32 s13, 0
	s_cbranch_scc1 .Lmy_rt_g5

;   __device__ __forceinline__ bool next(int i,AttnUnit&u)const{ const int pair=vcu+(i>>1)*G; if(pair>=256)return false; const int s=pair&15; u.bh=pair>>4; u.qb=(i&1)?31-s:s; return true; }
;     __device__ __forceinline__ bool next(int i, Unit& u) const { return i == 0 && so.next(round, u); }
; __global__ void __launch_bounds__(NWAVES * 64, 2) mega_fwd(Args args) {
;     ...
;               _Pragma("unroll 1") for (int i_ = 0; i_ < nu_; ++i_) { (void)S.next(i_, u_); const int pm_ = __builtin_amdgcn_readfirstlane(u_.pm);
;                   if (F.tid < 256) { const unsigned tk = (unsigned)rowtok[pm_ * 256 + F.tid]; RT[i_ * 256 + F.tid] = (int)(tk < (unsigned)T ? tk : (unsigned)(T - 1)); } } }
.Lmy_rt_d6:
	s_nop 0
	v_readfirstlane_b32 s18, v236
	s_and_saveexec_b64 s[10:11], s[0:1]
	v_lshl_add_u32 v4, s18, 8, v132
	v_ashrrev_i32_e32 v5, 31, v4
	v_lshl_add_u64 v[4:5], v[4:5], 2, s[4:5]
	global_load_dword v12, v[4:5], off
	s_or_b64 exec, exec, s[10:11]
	s_add_i32 s13, s13, -1
	s_add_i32 s17, s17, s14
	s_cmp_eq_u32 s13, 0
	s_cbranch_scc1 .Lmy_rt_g6

;   __device__ __forceinline__ bool next(int i,AttnUnit&u)const{ const int pair=vcu+(i>>1)*G; if(pair>=256)return false; const int s=pair&15; u.bh=pair>>4; u.qb=(i&1)?31-s:s; return true; }
;     __device__ __forceinline__ bool next(int i, Unit& u) const { return i == 0 && so.next(round, u); }
; __global__ void __launch_bounds__(NWAVES * 64, 2) mega_fwd(Args args) {
;     ...
;               _Pragma("unroll 1") for (int i_ = 0; i_ < nu_; ++i_) { (void)S.next(i_, u_); const int pm_ = __builtin_amdgcn_readfirstlane(u_.pm);
;                   if (F.tid < 256) { const unsigned tk = (unsigned)rowtok[pm_ * 256 + F.tid]; RT[i_ * 256 + F.tid] = (int)(tk < (unsigned)T ? tk : (unsigned)(T - 1)); } } }
.Lmy_rt_d7:
	s_nop 0
	v_readfirstlane_b32 s18, v236
	s_and_saveexec_b64 s[10:11], s[0:1]
	v_lshl_add_u32 v4, s18, 8, v132
	v_ashrrev_i32_e32 v5, 31, v4
	v_lshl_add_u64 v[4:5], v[4:5], 2, s[4:5]
	global_load_dword v13, v[4:5], off
	s_or_b64 exec, exec, s[10:11]
	s_add_i32 s13, s13, -1
	s_add_i32 s17, s17, s14
	s_cmp_eq_u32 s13, 0
	s_cbranch_scc1 .Lmy_rt_g7

;   __device__ __forceinline__ bool next(int i,AttnUnit&u)const{ const int pair=vcu+(i>>1)*G; if(pair>=256)return false; const int s=pair&15; u.bh=pair>>4; u.qb=(i&1)?31-s:s; return true; }
;     __device__ __forceinline__ bool next(int i, Unit& u) const { return i == 0 && so.next(round, u); }
; __global__ void __launch_bounds__(NWAVES * 64, 2) mega_fwd(Args args) {
;     ...
;               _Pragma("unroll 1") for (int i_ = 0; i_ < nu_; ++i_) { (void)S.next(i_, u_); const int pm_ = __builtin_amdgcn_readfirstlane(u_.pm);
;                   if (F.tid < 256) { const unsigned tk = (unsigned)rowtok[pm_ * 256 + F.tid]; RT[i_ * 256 + F.tid] = (int)(tk < (unsigned)T ? tk : (unsigned)(T - 1)); } } }
.Lmy_rt_d8:
	s_nop 0
	v_readfirstlane_b32 s18, v236
	s_and_saveexec_b64 s[10:11], s[0:1]
	v_lshl_add_u32 v4, s18, 8, v132
	v_ashrrev_i32_e32 v5, 31, v4
	v_lshl_add_u64 v[4:5], v[4:5], 2, s[4:5]
	global_load_dword v14, v[4:5], off
	s_or_b64 exec, exec, s[10:11]
	s_add_i32 s13, s13, -1
	s_add_i32 s17, s17, s14
	s_cmp_eq_u32 s13, 0
	s_cbranch_scc1 .Lmy_rt_g8

;   __device__ __forceinline__ bool next(int i,AttnUnit&u)const{ const int pair=vcu+(i>>1)*G; if(pair>=256)return false; const int s=pair&15; u.bh=pair>>4; u.qb=(i&1)?31-s:s; return true; }
;     __device__ __forceinline__ bool next(int i, Unit& u) const { return i == 0 && so.next(round, u); }
; __global__ void __launch_bounds__(NWAVES * 64, 2) mega_fwd(Args args) {
;     ...
;               _Pragma("unroll 1") for (int i_ = 0; i_ < nu_; ++i_) { (void)S.next(i_, u_); const int pm_ = __builtin_amdgcn_readfirstlane(u_.pm);
;                   if (F.tid < 256) { const unsigned tk = (unsigned)rowtok[pm_ * 256 + F.tid]; RT[i_ * 256 + F.tid] = (int)(tk < (unsigned)T ? tk : (unsigned)(T - 1)); } } }
.Lmy_rt_d9:
	s_nop 0
	v_readfirstlane_b32 s18, v236
	s_and_saveexec_b64 s[10:11], s[0:1]
	v_lshl_add_u32 v4, s18, 8, v132
	v_ashrrev_i32_e32 v5, 31, v4
	v_lshl_add_u64 v[4:5], v[4:5], 2, s[4:5]
	global_load_dword v15, v[4:5], off
	s_or_b64 exec, exec, s[10:11]
	s_add_i32 s13, s13, -1
	s_add_i32 s17, s17, s14
	s_cmp_eq_u32 s13, 0
	s_cbranch_scc1 .Lmy_rt_g9

;   __device__ __forceinline__ bool next(int i,AttnUnit&u)const{ const int pair=vcu+(i>>1)*G; if(pair>=256)return false; const int s=pair&15; u.bh=pair>>4; u.qb=(i&1)?31-s:s; return true; }
;     __device__ __forceinline__ bool next(int i, Unit& u) const { return i == 0 && so.next(round, u); }
; __global__ void __launch_bounds__(NWAVES * 64, 2) mega_fwd(Args args) {
;     ...
;               _Pragma("unroll 1") for (int i_ = 0; i_ < nu_; ++i_) { (void)S.next(i_, u_); const int pm_ = __builtin_amdgcn_readfirstlane(u_.pm);
;                   if (F.tid < 256) { const unsigned tk = (unsigned)rowtok[pm_ * 256 + F.tid]; RT[i_ * 256 + F.tid] = (int)(tk < (unsigned)T ? tk : (unsigned)(T - 1)); } } }
.Lmy_rt_d10:
	s_nop 0
	v_readfirstlane_b32 s18, v236
	s_and_saveexec_b64 s[10:11], s[0:1]
	v_lshl_add_u32 v4, s18, 8, v132
	v_ashrrev_i32_e32 v5, 31, v4
	v_lshl_add_u64 v[4:5], v[4:5], 2, s[4:5]
	global_load_dword v16, v[4:5], off
	s_or_b64 exec, exec, s[10:11]
	s_add_i32 s13, s13, -1
	s_add_i32 s17, s17, s14
	s_cmp_eq_u32 s13, 0
	s_cbranch_scc1 .Lmy_rt_g10

;   __device__ __forceinline__ bool next(int i,AttnUnit&u)const{ const int pair=vcu+(i>>1)*G; if(pair>=256)return false; const int s=pair&15; u.bh=pair>>4; u.qb=(i&1)?31-s:s; return true; }
;     __device__ __forceinline__ bool next(int i, Unit& u) const { return i == 0 && so.next(round, u); }
; __global__ void __launch_bounds__(NWAVES * 64, 2) mega_fwd(Args args) {
;     ...
;               _Pragma("unroll 1") for (int i_ = 0; i_ < nu_; ++i_) { (void)S.next(i_, u_); const int pm_ = __builtin_amdgcn_readfirstlane(u_.pm);
;                   if (F.tid < 256) { const unsigned tk = (unsigned)rowtok[pm_ * 256 + F.tid]; RT[i_ * 256 + F.tid] = (int)(tk < (unsigned)T ? tk : (unsigned)(T - 1)); } } }
.Lmy_rt_d11:
	s_nop 0
	v_readfirstlane_b32 s18, v236
	s_and_saveexec_b64 s[10:11], s[0:1]
	v_lshl_add_u32 v4, s18, 8, v132
	v_ashrrev_i32_e32 v5, 31, v4
	v_lshl_add_u64 v[4:5], v[4:5], 2, s[4:5]
	global_load_dword v17, v[4:5], off
	s_or_b64 exec, exec, s[10:11]
	s_add_i32 s13, s13, -1
	s_add_i32 s17, s17, s14
	s_cmp_eq_u32 s13, 0
	s_cbranch_scc1 .Lmy_rt_g11
.Lmy_rt_g11:
	s_waitcnt vmcnt(0)
	s_and_saveexec_b64 s[10:11], s[0:1]
	s_branch .Lmy_rt_w11

; __global__ void __launch_bounds__(NWAVES * 64, 2) mega_fwd(Args args) {
;     ...
;                   if (F.tid < 256) { const unsigned tk = (unsigned)rowtok[pm_ * 256 + F.tid]; RT[i_ * 256 + F.tid] = (int)(tk < (unsigned)T ? tk : (unsigned)(T - 1)); } } }
.Lmy_rt_w11:
	v_min_u32_e32 v0, 0x7fff, v17
	ds_write_b32 v1, v0 offset:11264
.Lmy_rt_w10:
	v_min_u32_e32 v0, 0x7fff, v16
	ds_write_b32 v1, v0 offset:10240
.Lmy_rt_w9:
	v_min_u32_e32 v0, 0x7fff, v15
	ds_write_b32 v1, v0 offset:9216
.Lmy_rt_w8:
	v_min_u32_e32 v0, 0x7fff, v14
	ds_write_b32 v1, v0 offset:8192
.Lmy_rt_w7:
	v_min_u32_e32 v0, 0x7fff, v13
	ds_write_b32 v1, v0 offset:7168
.Lmy_rt_w6:
	v_min_u32_e32 v0, 0x7fff, v12
	ds_write_b32 v1, v0 offset:6144
.Lmy_rt_w5:
	v_min_u32_e32 v0, 0x7fff, v11
	ds_write_b32 v1, v0 offset:5120
.Lmy_rt_w4:
	v_min_u32_e32 v0, 0x7fff, v10
	ds_write_b32 v1, v0 offset:4096
.Lmy_rt_w3:
	v_min_u32_e32 v0, 0x7fff, v9
	ds_write_b32 v1, v0 offset:3072
.Lmy_rt_w2:
	v_min_u32_e32 v0, 0x7fff, v8
	ds_write_b32 v1, v0 offset:2048
.Lmy_rt_w1:
	v_min_u32_e32 v0, 0x7fff, v7
	ds_write_b32 v1, v0 offset:1024
.Lmy_rt_w0:
	v_min_u32_e32 v0, 0x7fff, v6
	ds_write_b32 v1, v0
	s_or_b64 exec, exec, s[10:11]
